# v13 + z rope epilogue: per-row sum-of-squares cross-lane reduction via permlane16/32 swap instead of two LDS bpermute round trips per row
# speedup vs baseline: 1.0031x; 1.0031x over previous
.LBB0_502:
	s_lshl_b32 s9, s14, 8
	s_lshl_b32 s14, s8, 1
	s_add_i32 s14, s14, -12
	s_cmp_gt_i32 s8, 5
	s_cselect_b32 s14, s14, 0
	s_lshl_b64 s[30:31], s[14:15], 21
	s_add_u32 s30, s30, 0x1800000
	s_addc_u32 s31, s31, 0
	s_add_i32 s14, s8, -10
	v_add_u32_e32 v158, s9, v165
	s_cmp_gt_u32 s14, -5
	s_mov_b64 s[34:35], -1
	s_cbranch_scc0 .LBB0_537
	s_and_b32 s14, s8, 14
	s_cmp_eq_u32 s14, 6
	s_cselect_b32 s35, s71, s73
	s_cselect_b32 s34, s70, s72
	v_ashrrev_i32_e32 v159, 31, v158
	v_lshl_add_u64 v[130:131], s[34:35], 0, v[146:147]
	v_lshl_add_u64 v[194:195], v[158:159], 2, s[0:1]
	flat_load_dwordx4 v[134:137], v[130:131]
	s_nop 0
	flat_load_dwordx4 v[130:133], v[130:131] offset:256
	s_nop 0
	flat_load_dword v160, v[194:195]
	flat_load_dword v161, v[194:195] offset:64
	flat_load_dword v186, v[194:195] offset:128
	flat_load_dword v187, v[194:195] offset:192
	flat_load_dword v188, v[194:195] offset:512
	flat_load_dword v191, v[194:195] offset:576
	flat_load_dword v192, v[194:195] offset:640
	flat_load_dword v193, v[194:195] offset:704
	v_and_b32_e32 v189, 64, v185
	v_xor_b32_e32 v166, 16, v185
	v_add_u32_e32 v190, 64, v189
	v_cmp_lt_i32_e32 vcc, v166, v190
	v_mul_f32_e32 v194, v129, v129
	v_fmac_f32_e32 v194, v128, v128
	v_cndmask_b32_e32 v166, v185, v166, vcc
	v_lshlrev_b32_e32 v189, 2, v166
	v_mul_f32_e32 v166, v127, v127
	v_fmac_f32_e32 v166, v126, v126
	v_add_f32_e32 v166, v166, v194
	v_mul_f32_e32 v194, v123, v123
	v_fmac_f32_e32 v194, v122, v122
	v_add_f32_e32 v166, v166, v194
	v_mul_f32_e32 v194, v125, v125
	v_fmac_f32_e32 v194, v124, v124
	v_add_f32_e32 v166, v194, v166
	v_mov_b32_e32 v195, v166
	s_nop 1
	v_permlane16_swap_b32 v166, v195
	v_xor_b32_e32 v194, 32, v185
	v_cmp_lt_i32_e32 vcc, v194, v190
	s_waitcnt lgkmcnt(0)
	v_add_f32_e32 v195, v166, v195
	v_cndmask_b32_e32 v190, v185, v194, vcc
	v_lshlrev_b32_e32 v194, 2, v190
	v_mov_b32_e32 v196, v195
	s_nop 1
	v_permlane32_swap_b32 v195, v196
	v_add_u32_e32 v190, s83, v168
	s_and_saveexec_b64 s[34:35], s[4:5]
	s_cbranch_execz .LBB0_505
	v_add_f32_e32 v166, v195, v196
	ds_write_b32 v190, v166
.LBB0_505:
	s_or_b64 exec, exec, s[34:35]
	v_mul_f32_e32 v166, v119, v119
	v_mul_f32_e32 v195, v121, v121
	v_fmac_f32_e32 v166, v118, v118
	v_fmac_f32_e32 v195, v120, v120
	v_add_f32_e32 v166, v166, v195
	v_mul_f32_e32 v195, v115, v115
	v_fmac_f32_e32 v195, v114, v114
	v_add_f32_e32 v166, v166, v195
	v_mul_f32_e32 v195, v117, v117
	v_fmac_f32_e32 v195, v116, v116
	v_add_f32_e32 v166, v195, v166
	v_mov_b32_e32 v195, v166
	s_nop 1
	v_permlane16_swap_b32 v166, v195
	v_add_f32_e32 v195, v166, v195
	v_mov_b32_e32 v196, v195
	s_nop 1
	v_permlane32_swap_b32 v195, v196
	s_and_saveexec_b64 s[34:35], s[4:5]
	s_cbranch_execz .LBB0_507
	v_add_f32_e32 v166, v195, v196
	ds_write_b32 v190, v166 offset:16
.LBB0_507:
	s_or_b64 exec, exec, s[34:35]
	v_mul_f32_e32 v166, v111, v111
	v_mul_f32_e32 v195, v113, v113
	v_fmac_f32_e32 v166, v110, v110
	v_fmac_f32_e32 v195, v112, v112
	v_add_f32_e32 v166, v166, v195
	v_mul_f32_e32 v195, v107, v107
	v_fmac_f32_e32 v195, v106, v106
	v_add_f32_e32 v166, v166, v195
	v_mul_f32_e32 v195, v109, v109
	v_fmac_f32_e32 v195, v108, v108
	v_add_f32_e32 v166, v195, v166
	v_mov_b32_e32 v195, v166
	s_nop 1
	v_permlane16_swap_b32 v166, v195
	v_add_f32_e32 v195, v166, v195
	v_mov_b32_e32 v196, v195
	s_nop 1
	v_permlane32_swap_b32 v195, v196
	s_and_saveexec_b64 s[34:35], s[4:5]
	s_cbranch_execz .LBB0_509
	v_add_f32_e32 v166, v195, v196
	ds_write_b32 v190, v166 offset:512
.LBB0_509:
	s_or_b64 exec, exec, s[34:35]
	v_mul_f32_e32 v166, v103, v103
	v_mul_f32_e32 v195, v105, v105
	v_fmac_f32_e32 v166, v102, v102
	v_fmac_f32_e32 v195, v104, v104
	v_add_f32_e32 v166, v166, v195
	v_mul_f32_e32 v195, v99, v99
	v_fmac_f32_e32 v195, v98, v98
	v_add_f32_e32 v166, v166, v195
	v_mul_f32_e32 v195, v101, v101
	v_fmac_f32_e32 v195, v100, v100
	v_add_f32_e32 v166, v195, v166
	v_mov_b32_e32 v195, v166
	s_nop 1
	v_permlane16_swap_b32 v166, v195
	v_add_f32_e32 v195, v166, v195
	v_mov_b32_e32 v196, v195
	s_nop 1
	v_permlane32_swap_b32 v195, v196
	s_and_saveexec_b64 s[34:35], s[4:5]
	s_cbranch_execz .LBB0_511
	v_add_f32_e32 v166, v195, v196
	ds_write_b32 v190, v166 offset:528
.LBB0_511:
	s_or_b64 exec, exec, s[34:35]
	v_mul_f32_e32 v166, v95, v95
	v_mul_f32_e32 v195, v97, v97
	v_fmac_f32_e32 v166, v94, v94
	v_fmac_f32_e32 v195, v96, v96
	v_add_f32_e32 v166, v166, v195
	v_mul_f32_e32 v195, v91, v91
	v_fmac_f32_e32 v195, v90, v90
	v_add_f32_e32 v166, v166, v195
	v_mul_f32_e32 v195, v93, v93
	v_fmac_f32_e32 v195, v92, v92
	v_add_f32_e32 v166, v195, v166
	v_mov_b32_e32 v195, v166
	s_nop 1
	v_permlane16_swap_b32 v166, v195
	v_add_f32_e32 v195, v166, v195
	v_mov_b32_e32 v196, v195
	s_nop 1
	v_permlane32_swap_b32 v195, v196
	s_and_saveexec_b64 s[34:35], s[4:5]
	s_cbranch_execz .LBB0_513
	v_add_f32_e32 v166, v195, v196
	ds_write_b32 v190, v166 offset:1024
.LBB0_513:
	s_or_b64 exec, exec, s[34:35]
	v_mul_f32_e32 v166, v87, v87
	v_mul_f32_e32 v195, v89, v89
	v_fmac_f32_e32 v166, v86, v86
	v_fmac_f32_e32 v195, v88, v88
	v_add_f32_e32 v166, v166, v195
	v_mul_f32_e32 v195, v83, v83
	v_fmac_f32_e32 v195, v82, v82
	v_add_f32_e32 v166, v166, v195
	v_mul_f32_e32 v195, v85, v85
	v_fmac_f32_e32 v195, v84, v84
	v_add_f32_e32 v166, v195, v166
	v_mov_b32_e32 v195, v166
	s_nop 1
	v_permlane16_swap_b32 v166, v195
	v_add_f32_e32 v195, v166, v195
	v_mov_b32_e32 v196, v195
	s_nop 1
	v_permlane32_swap_b32 v195, v196
	s_and_saveexec_b64 s[34:35], s[4:5]
	s_cbranch_execz .LBB0_515
	v_add_f32_e32 v166, v195, v196
	ds_write_b32 v190, v166 offset:1040
.LBB0_515:
	s_or_b64 exec, exec, s[34:35]
	v_mul_f32_e32 v166, v79, v79
	v_mul_f32_e32 v195, v81, v81
	v_fmac_f32_e32 v166, v78, v78
	v_fmac_f32_e32 v195, v80, v80
	v_add_f32_e32 v166, v166, v195
	v_mul_f32_e32 v195, v75, v75
	v_fmac_f32_e32 v195, v74, v74
	v_add_f32_e32 v166, v166, v195
	v_mul_f32_e32 v195, v77, v77
	v_fmac_f32_e32 v195, v76, v76
	v_add_f32_e32 v166, v195, v166
	v_mov_b32_e32 v195, v166
	s_nop 1
	v_permlane16_swap_b32 v166, v195
	v_add_f32_e32 v195, v166, v195
	v_mov_b32_e32 v196, v195
	s_nop 1
	v_permlane32_swap_b32 v195, v196
	s_and_saveexec_b64 s[34:35], s[4:5]
	s_cbranch_execz .LBB0_517
	v_add_f32_e32 v166, v195, v196
	ds_write_b32 v190, v166 offset:1536
.LBB0_517:
	s_or_b64 exec, exec, s[34:35]
	v_mul_f32_e32 v166, v71, v71
	v_mul_f32_e32 v195, v73, v73
	v_fmac_f32_e32 v166, v70, v70
	v_fmac_f32_e32 v195, v72, v72
	v_add_f32_e32 v166, v166, v195
	v_mul_f32_e32 v195, v67, v67
	v_fmac_f32_e32 v195, v66, v66
	v_add_f32_e32 v166, v166, v195
	v_mul_f32_e32 v195, v69, v69
	v_fmac_f32_e32 v195, v68, v68
	v_add_f32_e32 v166, v195, v166
	v_mov_b32_e32 v195, v166
	s_nop 1
	v_permlane16_swap_b32 v166, v195
	v_add_f32_e32 v195, v166, v195
	v_mov_b32_e32 v196, v195
	s_nop 1
	v_permlane32_swap_b32 v195, v196
	s_and_saveexec_b64 s[34:35], s[4:5]
	s_cbranch_execz .LBB0_519
	v_add_f32_e32 v166, v195, v196
	ds_write_b32 v190, v166 offset:1552
.LBB0_519:
	s_or_b64 exec, exec, s[34:35]
	v_mul_f32_e32 v166, v63, v63
	v_mul_f32_e32 v195, v65, v65
	v_fmac_f32_e32 v166, v62, v62
	v_fmac_f32_e32 v195, v64, v64
	v_add_f32_e32 v166, v166, v195
	v_mul_f32_e32 v195, v59, v59
	v_fmac_f32_e32 v195, v58, v58
	v_add_f32_e32 v166, v166, v195
	v_mul_f32_e32 v195, v61, v61
	v_fmac_f32_e32 v195, v60, v60
	v_add_f32_e32 v166, v195, v166
	v_mov_b32_e32 v195, v166
	s_nop 1
	v_permlane16_swap_b32 v166, v195
	v_add_f32_e32 v195, v166, v195
	v_mov_b32_e32 v196, v195
	s_nop 1
	v_permlane32_swap_b32 v195, v196
	s_and_saveexec_b64 s[34:35], s[4:5]
	s_cbranch_execz .LBB0_521
	v_add_f32_e32 v166, v195, v196
	ds_write_b32 v190, v166 offset:4096
.LBB0_521:
	s_or_b64 exec, exec, s[34:35]
	v_mul_f32_e32 v166, v55, v55
	v_mul_f32_e32 v195, v57, v57
	v_fmac_f32_e32 v166, v54, v54
	v_fmac_f32_e32 v195, v56, v56
	v_add_f32_e32 v166, v166, v195
	v_mul_f32_e32 v195, v51, v51
	v_fmac_f32_e32 v195, v50, v50
	v_add_f32_e32 v166, v166, v195
	v_mul_f32_e32 v195, v53, v53
	v_fmac_f32_e32 v195, v52, v52
	v_add_f32_e32 v166, v195, v166
	v_mov_b32_e32 v195, v166
	s_nop 1
	v_permlane16_swap_b32 v166, v195
	v_add_f32_e32 v195, v166, v195
	v_mov_b32_e32 v196, v195
	s_nop 1
	v_permlane32_swap_b32 v195, v196
	s_and_saveexec_b64 s[34:35], s[4:5]
	s_cbranch_execz .LBB0_523
	v_add_f32_e32 v166, v195, v196
	ds_write_b32 v190, v166 offset:4112
.LBB0_523:
	s_or_b64 exec, exec, s[34:35]
	v_mul_f32_e32 v166, v47, v47
	v_mul_f32_e32 v195, v49, v49
	v_fmac_f32_e32 v166, v46, v46
	v_fmac_f32_e32 v195, v48, v48
	v_add_f32_e32 v166, v166, v195
	v_mul_f32_e32 v195, v43, v43
	v_fmac_f32_e32 v195, v42, v42
	v_add_f32_e32 v166, v166, v195
	v_mul_f32_e32 v195, v45, v45
	v_fmac_f32_e32 v195, v44, v44
	v_add_f32_e32 v166, v195, v166
	v_mov_b32_e32 v195, v166
	s_nop 1
	v_permlane16_swap_b32 v166, v195
	v_add_f32_e32 v195, v166, v195
	v_mov_b32_e32 v196, v195
	s_nop 1
	v_permlane32_swap_b32 v195, v196
	s_and_saveexec_b64 s[34:35], s[4:5]
	s_cbranch_execz .LBB0_525
	v_add_f32_e32 v166, v195, v196
	ds_write_b32 v190, v166 offset:4608
.LBB0_525:
	s_or_b64 exec, exec, s[34:35]
	v_mul_f32_e32 v166, v39, v39
	v_mul_f32_e32 v195, v41, v41
	v_fmac_f32_e32 v166, v38, v38
	v_fmac_f32_e32 v195, v40, v40
	v_add_f32_e32 v166, v166, v195
	v_mul_f32_e32 v195, v35, v35
	v_fmac_f32_e32 v195, v34, v34
	v_add_f32_e32 v166, v166, v195
	v_mul_f32_e32 v195, v37, v37
	v_fmac_f32_e32 v195, v36, v36
	v_add_f32_e32 v166, v195, v166
	v_mov_b32_e32 v195, v166
	s_nop 1
	v_permlane16_swap_b32 v166, v195
	v_add_f32_e32 v195, v166, v195
	v_mov_b32_e32 v196, v195
	s_nop 1
	v_permlane32_swap_b32 v195, v196
	s_and_saveexec_b64 s[34:35], s[4:5]
	s_cbranch_execz .LBB0_527
	v_add_f32_e32 v166, v195, v196
	ds_write_b32 v190, v166 offset:4624
.LBB0_527:
	s_or_b64 exec, exec, s[34:35]
	v_mul_f32_e32 v166, v31, v31
	v_mul_f32_e32 v195, v33, v33
	v_fmac_f32_e32 v166, v30, v30
	v_fmac_f32_e32 v195, v32, v32
	v_add_f32_e32 v166, v166, v195
	v_mul_f32_e32 v195, v27, v27
	v_fmac_f32_e32 v195, v26, v26
	v_add_f32_e32 v166, v166, v195
	v_mul_f32_e32 v195, v29, v29
	v_fmac_f32_e32 v195, v28, v28
	v_add_f32_e32 v166, v195, v166
	v_mov_b32_e32 v195, v166
	s_nop 1
	v_permlane16_swap_b32 v166, v195
	v_add_f32_e32 v195, v166, v195
	v_mov_b32_e32 v196, v195
	s_nop 1
	v_permlane32_swap_b32 v195, v196
	s_and_saveexec_b64 s[34:35], s[4:5]
	s_cbranch_execz .LBB0_529
	v_add_f32_e32 v166, v195, v196
	ds_write_b32 v190, v166 offset:5120
.LBB0_529:
	s_or_b64 exec, exec, s[34:35]
	v_mul_f32_e32 v166, v23, v23
	v_mul_f32_e32 v195, v25, v25
	v_fmac_f32_e32 v166, v22, v22
	v_fmac_f32_e32 v195, v24, v24
	v_add_f32_e32 v166, v166, v195
	v_mul_f32_e32 v195, v19, v19
	v_fmac_f32_e32 v195, v18, v18
	v_add_f32_e32 v166, v166, v195
	v_mul_f32_e32 v195, v21, v21
	v_fmac_f32_e32 v195, v20, v20
	v_add_f32_e32 v166, v195, v166
	v_mov_b32_e32 v195, v166
	s_nop 1
	v_permlane16_swap_b32 v166, v195
	v_add_f32_e32 v195, v166, v195
	v_mov_b32_e32 v196, v195
	s_nop 1
	v_permlane32_swap_b32 v195, v196
	s_and_saveexec_b64 s[34:35], s[4:5]
	s_cbranch_execz .LBB0_531
	v_add_f32_e32 v166, v195, v196
	ds_write_b32 v190, v166 offset:5136
.LBB0_531:
	s_or_b64 exec, exec, s[34:35]
	v_mul_f32_e32 v166, v15, v15
	v_mul_f32_e32 v195, v17, v17
	v_fmac_f32_e32 v166, v14, v14
	v_fmac_f32_e32 v195, v16, v16
	v_add_f32_e32 v166, v166, v195
	v_mul_f32_e32 v195, v11, v11
	v_fmac_f32_e32 v195, v10, v10
	v_add_f32_e32 v166, v166, v195
	v_mul_f32_e32 v195, v13, v13
	v_fmac_f32_e32 v195, v12, v12
	v_add_f32_e32 v166, v195, v166
	v_mov_b32_e32 v195, v166
	s_nop 1
	v_permlane16_swap_b32 v166, v195
	v_add_f32_e32 v195, v166, v195
	v_mov_b32_e32 v196, v195
	s_nop 1
	v_permlane32_swap_b32 v195, v196
	s_and_saveexec_b64 s[34:35], s[4:5]
	s_cbranch_execz .LBB0_533
	v_add_f32_e32 v166, v195, v196
	ds_write_b32 v190, v166 offset:5632
.LBB0_533:
	s_or_b64 exec, exec, s[34:35]
	v_mul_f32_e32 v166, v7, v7
	v_mul_f32_e32 v195, v9, v9
	v_fmac_f32_e32 v166, v6, v6
	v_fmac_f32_e32 v195, v8, v8
	v_add_f32_e32 v166, v166, v195
	v_mul_f32_e32 v195, v3, v3
	v_fmac_f32_e32 v195, v2, v2
	v_add_f32_e32 v166, v166, v195
	v_mul_f32_e32 v195, v5, v5
	v_fmac_f32_e32 v195, v4, v4
	v_add_f32_e32 v166, v195, v166
	v_mov_b32_e32 v189, v166
	s_nop 1
	v_permlane16_swap_b32 v166, v189
	v_add_f32_e32 v189, v166, v189
	v_mov_b32_e32 v194, v189
	s_nop 1
	v_permlane32_swap_b32 v189, v194
	s_and_saveexec_b64 s[34:35], s[4:5]
	s_cbranch_execz .LBB0_535
	v_add_f32_e32 v166, v189, v194
	ds_write_b32 v190, v166 offset:5648
